# stack: final-phase rewrite + MLA conflict-free K swizzles + MoE gate/up unit set-up (expert-id reuse, parallel index loads) + packed-f32 SwiGLU fp8 epilogue
# speedup vs baseline: 1.0105x; 1.0072x over previous
.LBB0_1711:
	s_mul_i32 s3, s68, 28
	s_ashr_i32 s2, s3, 31
	s_lshr_b32 s2, s2, 29
	s_add_i32 s8, s3, s2
	s_ashr_i32 s2, s8, 3
	s_and_b32 s8, s8, -8
	s_sub_i32 s3, s3, s8
	v_readlane_b32 s8, v252, 35
	s_cmp_lt_i32 s8, s3
	s_cselect_b64 s[8:9], -1, 0
	s_cmp_lg_u64 s[8:9], 0
	s_addc_u32 s73, s2, 0
	s_cmp_ge_i32 s1, s73
	s_cbranch_scc1 .LBB0_1736
	v_readlane_b32 s8, v252, 35
	s_mul_i32 s74, s2, s8
	s_min_i32 s2, s8, s3
	s_add_i32 s74, s74, s2
	s_add_i32 s1, s1, s74
	s_mul_hi_i32 s2, s1, 0x92492493
	s_add_i32 s2, s2, s1
	s_lshr_b32 s3, s2, 31
	s_ashr_i32 s2, s2, 7
	s_add_i32 s2, s2, s3
	s_lshl_b32 s3, s2, 3
	s_sub_i32 s8, s68, s3
	s_min_i32 s8, s8, 8
	s_abs_i32 s9, s8
	v_cvt_f32_u32_e32 v2, s9
	s_sub_i32 s13, 0, s9
	s_mulk_i32 s2, 0xe0
	s_sub_i32 s1, s1, s2
	v_rcp_iflag_f32_e32 v2, v2
	s_abs_i32 s2, s1
	s_xor_b32 s12, s1, s8
	s_ashr_i32 s12, s12, 31
	v_mul_f32_e32 v2, 0x4f7ffffe, v2
	v_cvt_u32_f32_e32 v2, v2
	s_nop 0
	v_readfirstlane_b32 s16, v2
	s_mul_i32 s13, s13, s16
	s_mul_hi_u32 s13, s16, s13
	s_add_i32 s16, s16, s13
	s_mul_hi_u32 s13, s2, s16
	s_mul_i32 s16, s13, s9
	s_sub_i32 s2, s2, s16
	s_add_i32 s17, s13, 1
	s_sub_i32 s16, s2, s9
	s_cmp_ge_u32 s2, s9
	s_cselect_b32 s13, s17, s13
	s_cselect_b32 s2, s16, s2
	s_add_i32 s16, s13, 1
	s_cmp_ge_u32 s2, s9
	s_cselect_b32 s2, s16, s13
	s_xor_b32 s2, s2, s12
	s_sub_i32 s46, s2, s12
	s_mul_i32 s2, s46, s8
	v_readlane_b32 s8, v252, 47
	v_readlane_b32 s9, v252, 48
	s_sub_i32 s1, s1, s2
	s_andn2_b64 vcc, exec, s[8:9]
	v_cndmask_b32_e64 v2, 0, 1, s[8:9]
	v_cmp_ne_u32_e64 s[38:39], 1, v2
	s_add_i32 s48, s1, s3
	s_mov_b32 s101, -1
	s_cbranch_vccnz .LBB0_1714
	s_ashr_i32 s49, s48, 31
	s_lshl_b64 s[2:3], s[48:49], 2
	s_add_u32 s2, s40, s2
	s_addc_u32 s3, s41, s3
	global_load_dword v2, v203, s[2:3]
	s_waitcnt vmcnt(0)
	v_readfirstlane_b32 s1, v2
	s_mov_b32 s100, s1
	s_mov_b32 s101, s48
	s_mul_hi_i32 s3, s1, 0x700000
	s_mul_i32 s2, s1, 0x700000
	s_branch .LBB0_1715

.LBB0_1722:
	v_cndmask_b32_e64 v130, 0, 1, s[50:51]
	v_cmp_ne_u32_e64 s[2:3], 1, v130
	s_andn2_b64 vcc, exec, s[50:51]
	s_mov_b64 s[50:51], s[22:23]
	v_mov_b32_e32 v173, v175
	v_mov_b32_e32 v169, v172
	v_mov_b32_e32 v170, v174
	v_mov_b32_e32 v168, v171
	s_cbranch_vccnz .LBB0_1728
	s_and_b64 vcc, exec, s[38:39]
	s_cbranch_vccnz .LBB0_1725
	s_ashr_i32 s45, s44, 31
	s_cmp_eq_u32 s44, s101
	s_cbranch_scc1 .Lgu_texp_hit
	s_lshl_b64 s[0:1], s[44:45], 2
	s_add_u32 s0, s40, s0
	s_addc_u32 s1, s41, s1
	global_load_dword v130, v203, s[0:1]
	s_waitcnt vmcnt(0)
	v_readfirstlane_b32 s100, v130
	s_mov_b32 s101, s44
.Lgu_texp_hit:
	s_mul_hi_i32 s51, s100, 0x700000
	s_mul_i32 s50, s100, 0x700000
	s_branch .LBB0_1726

.LBB0_1726:
	s_add_u32 s16, s61, s50
	s_addc_u32 s17, s62, s51
	s_ashr_i32 s43, s42, 31
	s_lshl_b64 s[0:1], s[42:43], 18
	s_add_u32 s50, s16, s0
	s_addc_u32 s51, s17, s1
	s_cmp_eq_u32 s44, s48
	v_mov_b32_e32 v173, v175
	v_mov_b32_e32 v169, v172
	v_mov_b32_e32 v170, v174
	v_mov_b32_e32 v168, v171
	s_cbranch_scc1 .LBB0_1728
	v_mov_b32_e32 v130, v1
	s_lshl_b32 s0, s44, 8
	s_or_b32 s1, s0, 0x80
	v_ashrrev_i32_e32 v131, 31, v130
	v_lshrrev_b32_e32 v131, 26, v131
	v_lshlrev_b32_e32 v132, 4, v130
	v_add_u32_e32 v131, v130, v131
	v_bfe_i32 v130, v130, 27, 1
	v_lshrrev_b32_e32 v130, 22, v130
	v_add_u32_e32 v130, v132, v130
	v_and_b32_e32 v130, 0xfffffc00, v130
	v_sub_u32_e32 v130, v132, v130
	v_lshrrev_b32_e32 v133, 4, v130
	v_bitop3_b32 v130, v133, v130, 32 bitop3:0x6c
	v_ashrrev_i32_e32 v134, 31, v130
	v_lshrrev_b32_e32 v134, 26, v134
	v_add_u32_e32 v134, v130, v134
	v_ashrrev_i32_e32 v131, 6, v131
	v_ashrrev_i32_e32 v135, 6, v134
	v_and_b32_e32 v134, 0xc0, v134
	v_lshlrev_b32_e32 v133, 3, v131
	v_sub_u32_e32 v130, v130, v134
	v_and_b32_e32 v133, -16, v133
	v_lshlrev_b32_e32 v131, 5, v131
	v_ashrrev_i16_sdwa v130, v217, sext(v130) dst_sel:DWORD dst_unused:UNUSED_PAD src0_sel:DWORD src1_sel:BYTE_0
	v_and_b32_e32 v131, 32, v131
	v_bfe_i32 v130, v130, 0, 16
	v_add_u32_e32 v133, v135, v133
	v_add_lshl_u32 v134, v131, v130, 1
	v_add_u32_e32 v130, s0, v133
	v_ashrrev_i32_e32 v131, 31, v130
	v_lshl_add_u64 v[130:131], v[130:131], 2, s[26:27]
	global_load_dword v136, v[130:131], off
	v_add_u32_e32 v130, s1, v133
	v_ashrrev_i32_e32 v131, 31, v130
	v_lshl_add_u64 v[130:131], v[130:131], 2, s[26:27]
	global_load_dword v137, v[130:131], off
	v_add_u32_e32 v140, 0x2000, v132
	v_ashrrev_i32_e32 v141, 31, v140
	v_lshrrev_b32_e32 v141, 22, v141
	v_add_u32_e32 v141, v140, v141
	v_ashrrev_i32_e32 v141, 10, v141
	v_mul_i32_i24_e32 v142, 0x400, v141
	v_sub_u32_e32 v140, v140, v142
	v_lshrrev_b32_e32 v142, 4, v140
	v_bitop3_b32 v140, v142, v140, 32 bitop3:0x6c
	v_ashrrev_i32_e32 v143, 31, v140
	v_lshrrev_b32_e32 v143, 26, v143
	v_add_u32_e32 v143, v140, v143
	v_ashrrev_i32_e32 v144, 6, v143
	v_and_b32_e32 v143, 0xc0, v143
	v_lshlrev_b32_e32 v142, 3, v141
	v_sub_u32_e32 v140, v140, v143
	v_and_b32_e32 v142, -16, v142
	v_lshlrev_b32_e32 v141, 5, v141
	v_ashrrev_i16_sdwa v140, v217, sext(v140) dst_sel:DWORD dst_unused:UNUSED_PAD src0_sel:DWORD src1_sel:BYTE_0
	v_and_b32_e32 v141, 32, v141
	v_bfe_i32 v140, v140, 0, 16
	v_add_u32_e32 v142, v144, v142
	v_add_lshl_u32 v143, v141, v140, 1
	v_add_u32_e32 v140, s0, v142
	v_ashrrev_i32_e32 v141, 31, v140
	v_lshl_add_u64 v[140:141], v[140:141], 2, s[26:27]
	global_load_dword v138, v[140:141], off
	v_add_u32_e32 v140, s1, v142
	v_ashrrev_i32_e32 v141, 31, v140
	v_lshl_add_u64 v[140:141], v[140:141], 2, s[26:27]
	global_load_dword v139, v[140:141], off
	s_waitcnt vmcnt(0)
	v_max_i32_e32 v136, 0, v136
	v_max_i32_e32 v137, 0, v137
	v_max_i32_e32 v138, 0, v138
	v_max_i32_e32 v139, 0, v139
	v_lshl_add_u32 v168, v136, 10, v134
	v_lshl_add_u32 v169, v137, 10, v134
	v_lshl_add_u32 v170, v138, 10, v143
	v_lshl_add_u32 v173, v139, 10, v143

.LBB0_1732:
	s_ashr_i32 s49, s48, 31
	s_lshl_b64 s[0:1], s[48:49], 8
	s_add_u32 s0, s0, s82
	s_addc_u32 s1, s1, s92
	s_mulk_i32 s1, 0xe00
	s_mul_hi_u32 s16, s0, 0xe00
	s_add_i32 s16, s16, s1
	s_mulk_i32 s0, 0xe00
	s_add_u32 s0, s80, s0
	s_addc_u32 s1, s81, s16
	s_lshl_b32 s16, s46, 7
	s_ashr_i32 s17, s16, 31
	s_add_u32 s0, s0, s16
	s_addc_u32 s1, s1, s17
	s_add_u32 s0, s0, s83
	s_addc_u32 s1, s1, 0
	s_movk_i32 s16, 0xe00
	v_mov_b32_e32 v130, v164
	v_mov_b32_e32 v131, v165
	v_mul_lo_u32 v130, v130, s16
	v_lshl_add_u32 v202, v131, 3, v130
	v_pk_mul_f32 v[98:99], v[114:115], v[98:99]
	v_pk_mul_f32 v[100:101], v[116:117], v[100:101]
	v_pk_mul_f32 v[102:103], v[118:119], v[102:103]
	v_pk_mul_f32 v[104:105], v[120:121], v[104:105]
	v_exp_f32_e32 v114, v114
	v_exp_f32_e32 v115, v115
	v_exp_f32_e32 v116, v116
	v_exp_f32_e32 v117, v117
	v_exp_f32_e32 v118, v118
	v_exp_f32_e32 v119, v119
	v_exp_f32_e32 v120, v120
	v_exp_f32_e32 v121, v121
	v_pk_add_f32 v[114:115], v[114:115], 1.0 op_sel_hi:[1,0]
	v_pk_add_f32 v[116:117], v[116:117], 1.0 op_sel_hi:[1,0]
	v_pk_add_f32 v[118:119], v[118:119], 1.0 op_sel_hi:[1,0]
	v_pk_add_f32 v[120:121], v[120:121], 1.0 op_sel_hi:[1,0]
	v_rcp_f32_e32 v114, v114
	v_rcp_f32_e32 v115, v115
	v_rcp_f32_e32 v116, v116
	v_rcp_f32_e32 v117, v117
	v_rcp_f32_e32 v118, v118
	v_rcp_f32_e32 v119, v119
	v_rcp_f32_e32 v120, v120
	v_rcp_f32_e32 v121, v121
	v_pk_mul_f32 v[98:99], v[114:115], v[98:99]
	v_pk_mul_f32 v[100:101], v[116:117], v[100:101]
	v_pk_mul_f32 v[102:103], v[118:119], v[102:103]
	v_pk_mul_f32 v[104:105], v[120:121], v[104:105]
	v_cvt_pk_fp8_f32 v130, v98, v99
	v_cvt_pk_fp8_f32 v131, v102, v103
	v_cvt_pk_fp8_f32 v130, v100, v101 op_sel:[0,0,1]
	v_cvt_pk_fp8_f32 v131, v104, v105 op_sel:[0,0,1]
	global_store_dwordx2 v202, v[130:131], s[0:1]
	v_pk_mul_f32 v[106:107], v[122:123], v[106:107]
	v_pk_mul_f32 v[108:109], v[124:125], v[108:109]
	v_pk_mul_f32 v[110:111], v[126:127], v[110:111]
	v_pk_mul_f32 v[112:113], v[128:129], v[112:113]
	v_exp_f32_e32 v122, v122
	v_exp_f32_e32 v123, v123
	v_exp_f32_e32 v124, v124
	v_exp_f32_e32 v125, v125
	v_exp_f32_e32 v126, v126
	v_exp_f32_e32 v127, v127
	v_exp_f32_e32 v128, v128
	v_exp_f32_e32 v129, v129
	v_pk_add_f32 v[122:123], v[122:123], 1.0 op_sel_hi:[1,0]
	v_pk_add_f32 v[124:125], v[124:125], 1.0 op_sel_hi:[1,0]
	v_pk_add_f32 v[126:127], v[126:127], 1.0 op_sel_hi:[1,0]
	v_pk_add_f32 v[128:129], v[128:129], 1.0 op_sel_hi:[1,0]
	v_rcp_f32_e32 v122, v122
	v_rcp_f32_e32 v123, v123
	v_rcp_f32_e32 v124, v124
	v_rcp_f32_e32 v125, v125
	v_rcp_f32_e32 v126, v126
	v_rcp_f32_e32 v127, v127
	v_rcp_f32_e32 v128, v128
	v_rcp_f32_e32 v129, v129
	v_pk_mul_f32 v[106:107], v[122:123], v[106:107]
	v_pk_mul_f32 v[108:109], v[124:125], v[108:109]
	v_pk_mul_f32 v[110:111], v[126:127], v[110:111]
	v_pk_mul_f32 v[112:113], v[128:129], v[112:113]
	v_cvt_pk_fp8_f32 v134, v106, v107
	v_cvt_pk_fp8_f32 v135, v110, v111
	v_cvt_pk_fp8_f32 v134, v108, v109 op_sel:[0,0,1]
	v_cvt_pk_fp8_f32 v135, v112, v113 op_sel:[0,0,1]
	v_add_u32_e32 v133, 0xe000, v202
	global_store_dwordx2 v133, v[134:135], s[0:1]
	v_pk_mul_f32 v[66:67], v[82:83], v[66:67]
	v_pk_mul_f32 v[68:69], v[84:85], v[68:69]
	v_pk_mul_f32 v[70:71], v[86:87], v[70:71]
	v_pk_mul_f32 v[72:73], v[88:89], v[72:73]
	v_exp_f32_e32 v82, v82
	v_exp_f32_e32 v83, v83
	v_exp_f32_e32 v84, v84
	v_exp_f32_e32 v85, v85
	v_exp_f32_e32 v86, v86
	v_exp_f32_e32 v87, v87
	v_exp_f32_e32 v88, v88
	v_exp_f32_e32 v89, v89
	v_pk_add_f32 v[82:83], v[82:83], 1.0 op_sel_hi:[1,0]
	v_pk_add_f32 v[84:85], v[84:85], 1.0 op_sel_hi:[1,0]
	v_pk_add_f32 v[86:87], v[86:87], 1.0 op_sel_hi:[1,0]
	v_pk_add_f32 v[88:89], v[88:89], 1.0 op_sel_hi:[1,0]
	v_rcp_f32_e32 v82, v82
	v_rcp_f32_e32 v83, v83
	v_rcp_f32_e32 v84, v84
	v_rcp_f32_e32 v85, v85
	v_rcp_f32_e32 v86, v86
	v_rcp_f32_e32 v87, v87
	v_rcp_f32_e32 v88, v88
	v_rcp_f32_e32 v89, v89
	v_pk_mul_f32 v[66:67], v[82:83], v[66:67]
	v_pk_mul_f32 v[68:69], v[84:85], v[68:69]
	v_pk_mul_f32 v[70:71], v[86:87], v[70:71]
	v_pk_mul_f32 v[72:73], v[88:89], v[72:73]
	v_cvt_pk_fp8_f32 v130, v66, v67
	v_cvt_pk_fp8_f32 v131, v70, v71
	v_cvt_pk_fp8_f32 v130, v68, v69 op_sel:[0,0,1]
	v_cvt_pk_fp8_f32 v131, v72, v73 op_sel:[0,0,1]
	v_add_u32_e32 v132, 0x1c000, v202
	global_store_dwordx2 v132, v[130:131], s[0:1]
	v_pk_mul_f32 v[74:75], v[90:91], v[74:75]
	v_pk_mul_f32 v[76:77], v[92:93], v[76:77]
	v_pk_mul_f32 v[78:79], v[94:95], v[78:79]
	v_pk_mul_f32 v[80:81], v[96:97], v[80:81]
	v_exp_f32_e32 v90, v90
	v_exp_f32_e32 v91, v91
	v_exp_f32_e32 v92, v92
	v_exp_f32_e32 v93, v93
	v_exp_f32_e32 v94, v94
	v_exp_f32_e32 v95, v95
	v_exp_f32_e32 v96, v96
	v_exp_f32_e32 v97, v97
	v_pk_add_f32 v[90:91], v[90:91], 1.0 op_sel_hi:[1,0]
	v_pk_add_f32 v[92:93], v[92:93], 1.0 op_sel_hi:[1,0]
	v_pk_add_f32 v[94:95], v[94:95], 1.0 op_sel_hi:[1,0]
	v_pk_add_f32 v[96:97], v[96:97], 1.0 op_sel_hi:[1,0]
	v_rcp_f32_e32 v90, v90
	v_rcp_f32_e32 v91, v91
	v_rcp_f32_e32 v92, v92
	v_rcp_f32_e32 v93, v93
	v_rcp_f32_e32 v94, v94
	v_rcp_f32_e32 v95, v95
	v_rcp_f32_e32 v96, v96
	v_rcp_f32_e32 v97, v97
	v_pk_mul_f32 v[74:75], v[90:91], v[74:75]
	v_pk_mul_f32 v[76:77], v[92:93], v[76:77]
	v_pk_mul_f32 v[78:79], v[94:95], v[78:79]
	v_pk_mul_f32 v[80:81], v[96:97], v[80:81]
	v_cvt_pk_fp8_f32 v134, v74, v75
	v_cvt_pk_fp8_f32 v135, v78, v79
	v_cvt_pk_fp8_f32 v134, v76, v77 op_sel:[0,0,1]
	v_cvt_pk_fp8_f32 v135, v80, v81 op_sel:[0,0,1]
	v_add_u32_e32 v133, 0x2a000, v202
	global_store_dwordx2 v133, v[134:135], s[0:1]
	v_pk_mul_f32 v[34:35], v[50:51], v[34:35]
	v_pk_mul_f32 v[36:37], v[52:53], v[36:37]
	v_pk_mul_f32 v[38:39], v[54:55], v[38:39]
	v_pk_mul_f32 v[40:41], v[56:57], v[40:41]
	v_exp_f32_e32 v50, v50
	v_exp_f32_e32 v51, v51
	v_exp_f32_e32 v52, v52
	v_exp_f32_e32 v53, v53
	v_exp_f32_e32 v54, v54
	v_exp_f32_e32 v55, v55
	v_exp_f32_e32 v56, v56
	v_exp_f32_e32 v57, v57
	v_pk_add_f32 v[50:51], v[50:51], 1.0 op_sel_hi:[1,0]
	v_pk_add_f32 v[52:53], v[52:53], 1.0 op_sel_hi:[1,0]
	v_pk_add_f32 v[54:55], v[54:55], 1.0 op_sel_hi:[1,0]
	v_pk_add_f32 v[56:57], v[56:57], 1.0 op_sel_hi:[1,0]
	v_rcp_f32_e32 v50, v50
	v_rcp_f32_e32 v51, v51
	v_rcp_f32_e32 v52, v52
	v_rcp_f32_e32 v53, v53
	v_rcp_f32_e32 v54, v54
	v_rcp_f32_e32 v55, v55
	v_rcp_f32_e32 v56, v56
	v_rcp_f32_e32 v57, v57
	v_pk_mul_f32 v[34:35], v[50:51], v[34:35]
	v_pk_mul_f32 v[36:37], v[52:53], v[36:37]
	v_pk_mul_f32 v[38:39], v[54:55], v[38:39]
	v_pk_mul_f32 v[40:41], v[56:57], v[40:41]
	v_cvt_pk_fp8_f32 v130, v34, v35
	v_cvt_pk_fp8_f32 v131, v38, v39
	v_cvt_pk_fp8_f32 v130, v36, v37 op_sel:[0,0,1]
	v_cvt_pk_fp8_f32 v131, v40, v41 op_sel:[0,0,1]
	v_add_u32_e32 v132, 0x70000, v202
	global_store_dwordx2 v132, v[130:131], s[0:1]
	v_pk_mul_f32 v[42:43], v[58:59], v[42:43]
	v_pk_mul_f32 v[44:45], v[60:61], v[44:45]
	v_pk_mul_f32 v[46:47], v[62:63], v[46:47]
	v_pk_mul_f32 v[48:49], v[64:65], v[48:49]
	v_exp_f32_e32 v58, v58
	v_exp_f32_e32 v59, v59
	v_exp_f32_e32 v60, v60
	v_exp_f32_e32 v61, v61
	v_exp_f32_e32 v62, v62
	v_exp_f32_e32 v63, v63
	v_exp_f32_e32 v64, v64
	v_exp_f32_e32 v65, v65
	v_pk_add_f32 v[58:59], v[58:59], 1.0 op_sel_hi:[1,0]
	v_pk_add_f32 v[60:61], v[60:61], 1.0 op_sel_hi:[1,0]
	v_pk_add_f32 v[62:63], v[62:63], 1.0 op_sel_hi:[1,0]
	v_pk_add_f32 v[64:65], v[64:65], 1.0 op_sel_hi:[1,0]
	v_rcp_f32_e32 v58, v58
	v_rcp_f32_e32 v59, v59
	v_rcp_f32_e32 v60, v60
	v_rcp_f32_e32 v61, v61
	v_rcp_f32_e32 v62, v62
	v_rcp_f32_e32 v63, v63
	v_rcp_f32_e32 v64, v64
	v_rcp_f32_e32 v65, v65
	v_pk_mul_f32 v[42:43], v[58:59], v[42:43]
	v_pk_mul_f32 v[44:45], v[60:61], v[44:45]
	v_pk_mul_f32 v[46:47], v[62:63], v[46:47]
	v_pk_mul_f32 v[48:49], v[64:65], v[48:49]
	v_cvt_pk_fp8_f32 v134, v42, v43
	v_cvt_pk_fp8_f32 v135, v46, v47
	v_cvt_pk_fp8_f32 v134, v44, v45 op_sel:[0,0,1]
	v_cvt_pk_fp8_f32 v135, v48, v49 op_sel:[0,0,1]
	v_add_u32_e32 v133, 0x7e000, v202
	global_store_dwordx2 v133, v[134:135], s[0:1]
	v_pk_mul_f32 v[2:3], v[18:19], v[2:3]
	v_pk_mul_f32 v[4:5], v[20:21], v[4:5]
	v_pk_mul_f32 v[6:7], v[22:23], v[6:7]
	v_pk_mul_f32 v[8:9], v[24:25], v[8:9]
	v_exp_f32_e32 v18, v18
	v_exp_f32_e32 v19, v19
	v_exp_f32_e32 v20, v20
	v_exp_f32_e32 v21, v21
	v_exp_f32_e32 v22, v22
	v_exp_f32_e32 v23, v23
	v_exp_f32_e32 v24, v24
	v_exp_f32_e32 v25, v25
	v_pk_add_f32 v[18:19], v[18:19], 1.0 op_sel_hi:[1,0]
	v_pk_add_f32 v[20:21], v[20:21], 1.0 op_sel_hi:[1,0]
	v_pk_add_f32 v[22:23], v[22:23], 1.0 op_sel_hi:[1,0]
	v_pk_add_f32 v[24:25], v[24:25], 1.0 op_sel_hi:[1,0]
	v_rcp_f32_e32 v18, v18
	v_rcp_f32_e32 v19, v19
	v_rcp_f32_e32 v20, v20
	v_rcp_f32_e32 v21, v21
	v_rcp_f32_e32 v22, v22
	v_rcp_f32_e32 v23, v23
	v_rcp_f32_e32 v24, v24
	v_rcp_f32_e32 v25, v25
	v_pk_mul_f32 v[2:3], v[18:19], v[2:3]
	v_pk_mul_f32 v[4:5], v[20:21], v[4:5]
	v_pk_mul_f32 v[6:7], v[22:23], v[6:7]
	v_pk_mul_f32 v[8:9], v[24:25], v[8:9]
	v_cvt_pk_fp8_f32 v130, v2, v3
	v_cvt_pk_fp8_f32 v131, v6, v7
	v_cvt_pk_fp8_f32 v130, v4, v5 op_sel:[0,0,1]
	v_cvt_pk_fp8_f32 v131, v8, v9 op_sel:[0,0,1]
	v_add_u32_e32 v132, 0x8c000, v202
	global_store_dwordx2 v132, v[130:131], s[0:1]
	v_pk_mul_f32 v[10:11], v[26:27], v[10:11]
	v_pk_mul_f32 v[12:13], v[28:29], v[12:13]
	v_pk_mul_f32 v[14:15], v[30:31], v[14:15]
	v_pk_mul_f32 v[16:17], v[32:33], v[16:17]
	v_exp_f32_e32 v26, v26
	v_exp_f32_e32 v27, v27
	v_exp_f32_e32 v28, v28
	v_exp_f32_e32 v29, v29
	v_exp_f32_e32 v30, v30
	v_exp_f32_e32 v31, v31
	v_exp_f32_e32 v32, v32
	v_exp_f32_e32 v33, v33
	v_pk_add_f32 v[26:27], v[26:27], 1.0 op_sel_hi:[1,0]
	v_pk_add_f32 v[28:29], v[28:29], 1.0 op_sel_hi:[1,0]
	v_pk_add_f32 v[30:31], v[30:31], 1.0 op_sel_hi:[1,0]
	v_pk_add_f32 v[32:33], v[32:33], 1.0 op_sel_hi:[1,0]
	v_rcp_f32_e32 v26, v26
	v_rcp_f32_e32 v27, v27
	v_rcp_f32_e32 v28, v28
	v_rcp_f32_e32 v29, v29
	v_rcp_f32_e32 v30, v30
	v_rcp_f32_e32 v31, v31
	v_rcp_f32_e32 v32, v32
	v_rcp_f32_e32 v33, v33
	v_pk_mul_f32 v[10:11], v[26:27], v[10:11]
	v_pk_mul_f32 v[12:13], v[28:29], v[12:13]
	v_pk_mul_f32 v[14:15], v[30:31], v[14:15]
	v_pk_mul_f32 v[16:17], v[32:33], v[16:17]
	v_cvt_pk_fp8_f32 v134, v10, v11
	v_cvt_pk_fp8_f32 v135, v14, v15
	v_cvt_pk_fp8_f32 v134, v12, v13 op_sel:[0,0,1]
	v_cvt_pk_fp8_f32 v135, v16, v17 op_sel:[0,0,1]
	v_add_u32_e32 v133, 0x9a000, v202
	global_store_dwordx2 v133, v[134:135], s[0:1]
	v_mov_b32 v2, 0
	v_mov_b32 v3, 0
	v_mov_b32 v4, 0
	v_mov_b32 v5, 0
	s_and_b64 vcc, exec, s[2:3]
	s_mov_b64 s[2:3], -1
	v_mfma_f32_32x32x16_bf16 v[114:129], v[2:5], v[2:5], 0
	s_nop 0
	v_mfma_f32_32x32x16_bf16 v[82:97], v[2:5], v[2:5], 0
	s_nop 0
	v_mfma_f32_32x32x16_bf16 v[98:113], v[2:5], v[2:5], 0
	s_nop 0
	v_mfma_f32_32x32x16_bf16 v[66:81], v[2:5], v[2:5], 0
	s_nop 0
	v_mfma_f32_32x32x16_bf16 v[50:65], v[2:5], v[2:5], 0
	s_nop 0
	v_mfma_f32_32x32x16_bf16 v[18:33], v[2:5], v[2:5], 0
	s_nop 0
	v_mfma_f32_32x32x16_bf16 v[34:49], v[2:5], v[2:5], 0
	s_nop 0
	v_mfma_f32_32x32x16_bf16 v[2:17], v[2:5], v[2:5], 0
	s_cbranch_vccnz .LBB0_1719
	s_andn2_b64 vcc, exec, s[8:9]
	s_cbranch_vccnz .LBB0_1718
	s_barrier
	s_branch .LBB0_1718
